# final phase: lane-to-element remap so every store instruction writes a contiguous 1 KB (dwordx2 loads)
# baseline (speedup 1.0000x reference)
; __device__ __forceinline__ void phase_final(const bf16* H, float* out, const float* gain, int gw, int NGW, int lane) {
;     constexpr int NR = 4;
;     f32x4 gv[2][2];
; #pragma unroll
;     for (int j = 0; j < 2; ++j) { gv[j][0] = ((const f32x4*)gain)[2 * lane + 128 * j]; gv[j][1] = ((const f32x4*)gain)[2 * lane + 128 * j + 1]; }
;     for (int m0 = gw * NR; m0 < NTOK; m0 += NGW * NR) { u32x4 v[NR][2];
; #pragma unroll
;         for (int r = 0; r < NR; ++r)
; #pragma unroll
;             for (int j = 0; j < 2; ++j) v[r][j] = ((const u32x4*)(H + (size_t)(m0 + r) * DM))[lane + 64 * j];
; #pragma unroll
;         for (int r = 0; r < NR; ++r) { const float rstd = rsqrtf(wave_sum(ss_u4(v[r][0]) + ss_u4(v[r][1])) * (1.f / DM) + EPS);
;             f32x4* xr = (f32x4*)(out + (size_t)(m0 + r) * DM);
; #pragma unroll
;             for (int j = 0; j < 2; ++j) { const u32x4 w = v[r][j];
;                 xr[2 * lane + 128 * j] = (f32x4){bflo(w.x), bfhi(w.x), bflo(w.y), bfhi(w.y)} * rstd * gv[j][0];
;                 xr[2 * lane + 128 * j + 1] = (f32x4){bflo(w.z), bfhi(w.z), bflo(w.w), bfhi(w.w)} * rstd * gv[j][1]; } } }
.LBB0_1264:
	s_mov_b64 s[0:1], s[66:67]
	s_load_dword s0, s[0:1], 0x138
	s_waitcnt lgkmcnt(0)
	s_cmp_lt_i32 s0, 46
	s_cbranch_scc0 .LBB0_1269
	s_mov_b64 s[0:1], s[66:67]
	s_load_dword s0, s[0:1], 0x13c
	s_waitcnt lgkmcnt(0)
	s_cmp_lt_i32 s0, 46
	s_cbranch_scc1 .LBB0_1269
	s_lshl_b32 s0, s68, 3
	v_mbcnt_lo_u32_b32 v0, -1, 0
	v_mbcnt_hi_u32_b32 v0, -1, v0
	s_add_i32 s0, s0, s69
	v_add_u32_e32 v0, s70, v0
	s_cmpk_gt_i32 s0, 0x3fff
	s_cbranch_scc1 .LBB0_1269
	s_load_dwordx4 s[8:11], s[66:67], 0x120
	s_load_dwordx2 s[2:3], s[66:67], 0x130
	s_waitcnt vmcnt(0)
	v_and_b32_e32 v20, 63, v0
	v_lshlrev_b32_e32 v16, 4, v20
	s_lshl_b32 s6, s65, 5
	s_waitcnt lgkmcnt(0)
	global_load_dwordx4 v[0:3], v16, s[8:9] offset:1024
	global_load_dwordx4 v[4:7], v16, s[8:9]
	global_load_dwordx4 v[8:11], v16, s[8:9] offset:3072
	global_load_dwordx4 v[12:15], v16, s[8:9] offset:2048
	s_lshl_b32 s8, s0, 2
	s_ashr_i32 s9, s8, 31
	s_lshl_b64 s[0:1], s[8:9], 12
	s_add_u32 s0, s10, s0
	v_mov_b32_e32 v17, 0
	s_addc_u32 s1, s11, s1
	v_lshl_add_u64 v[18:19], s[0:1], 0, v[16:17]
	s_mov_b64 s[0:1], 0x3810
	s_ashr_i32 s7, s6, 31
	v_lshl_add_u64 v[32:33], v[18:19], 0, s[0:1]
	s_lshl_b64 s[10:11], s[6:7], 12
	s_lshl_b64 s[0:1], s[8:9], 11
	s_add_u32 s0, s2, s0
	v_lshlrev_b32_e32 v16, 3, v20
	s_addc_u32 s1, s3, s1
	v_lshl_add_u64 v[16:17], s[0:1], 0, v[16:17]
	s_mov_b64 s[0:1], 0x4d201c00
	v_lshl_add_u64 v[34:35], v[16:17], 0, s[0:1]
	s_mov_b32 s0, 0x358637bd
	s_lshl_b64 s[12:13], s[6:7], 11
	s_movk_i32 s7, 0xf000
	s_mov_b32 s14, 0x3a800000
	s_mov_b32 s9, 0x800000
	s_movk_i32 s15, 0xd000
	s_movk_i32 s16, 0xe000
	v_mov_b64_e32 v[36:37], s[0:1]
.LBB0_1268:
	v_add_co_u32_e32 v42, vcc, 0xfffff000, v34
	global_load_dwordx2 v[28:29], v[34:35], off offset:-2048
	global_load_dwordx2 v[30:31], v[34:35], off offset:-1536
	global_load_dwordx2 v[24:25], v[34:35], off offset:-3072
	global_load_dwordx2 v[26:27], v[34:35], off offset:-2560
	global_load_dwordx2 v[20:21], v[34:35], off offset:0
	global_load_dwordx2 v[22:23], v[34:35], off offset:512
	global_load_dwordx2 v[16:17], v[34:35], off offset:-1024
	global_load_dwordx2 v[18:19], v[34:35], off offset:-512
	v_addc_co_u32_e32 v43, vcc, -1, v35, vcc
	global_load_dwordx2 v[46:47], v[42:43], off offset:-2048
	global_load_dwordx2 v[48:49], v[42:43], off offset:-1536
	global_load_dwordx2 v[50:51], v[42:43], off offset:-3072
	global_load_dwordx2 v[52:53], v[42:43], off offset:-2560
	global_load_dwordx2 v[54:55], v[42:43], off offset:-1024
	global_load_dwordx2 v[56:57], v[42:43], off offset:-512
	global_load_dwordx2 v[58:59], v[34:35], off offset:-4096
	global_load_dwordx2 v[60:61], v[34:35], off offset:-3584
	v_add_co_u32_e64 v38, s[0:1], s15, v32
	s_add_i32 s8, s8, s6
	s_nop 0
	v_addc_co_u32_e64 v39, s[0:1], -1, v33, s[0:1]
	v_add_co_u32_e64 v40, s[0:1], s16, v32
	s_cmp_lt_i32 s8, 0x10000
	s_nop 0
	v_addc_co_u32_e64 v41, s[0:1], -1, v33, s[0:1]
	v_add_co_u32_e64 v44, s[0:1], s7, v32
	v_lshl_add_u64 v[34:35], v[34:35], 0, s[12:13]
	s_nop 0
	v_addc_co_u32_e64 v45, s[0:1], -1, v33, s[0:1]
	s_waitcnt vmcnt(14)
	v_lshlrev_b32_e32 v43, 16, v28
	v_and_b32_e32 v63, 0xffff0000, v28
	s_waitcnt vmcnt(12)
	v_and_b32_e32 v62, 0xffff0000, v24
	v_lshlrev_b32_e32 v65, 16, v29
	v_lshlrev_b32_e32 v64, 16, v25
	v_and_b32_e32 v29, 0xffff0000, v29
	v_and_b32_e32 v28, 0xffff0000, v25
	v_lshlrev_b32_e32 v25, 16, v30
	v_and_b32_e32 v67, 0xffff0000, v30
	v_and_b32_e32 v66, 0xffff0000, v26
	v_lshlrev_b32_e32 v69, 16, v31
	v_lshlrev_b32_e32 v68, 16, v27
	v_and_b32_e32 v31, 0xffff0000, v31
	v_and_b32_e32 v30, 0xffff0000, v27
	s_waitcnt vmcnt(10)
	v_lshlrev_b32_e32 v27, 16, v20
	v_and_b32_e32 v71, 0xffff0000, v20
	s_waitcnt vmcnt(8)
	v_and_b32_e32 v70, 0xffff0000, v16
	v_lshlrev_b32_e32 v73, 16, v21
	v_lshlrev_b32_e32 v72, 16, v17
	v_and_b32_e32 v21, 0xffff0000, v21
	v_and_b32_e32 v20, 0xffff0000, v17
	v_lshlrev_b32_e32 v17, 16, v22
	v_and_b32_e32 v75, 0xffff0000, v22
	v_and_b32_e32 v74, 0xffff0000, v18
	v_lshlrev_b32_e32 v77, 16, v23
	v_and_b32_e32 v23, 0xffff0000, v23
	v_and_b32_e32 v22, 0xffff0000, v19
	v_lshlrev_b32_e32 v42, 16, v24
	v_lshlrev_b32_e32 v24, 16, v26
	v_lshlrev_b32_e32 v26, 16, v16
	v_lshlrev_b32_e32 v16, 16, v18
	v_lshlrev_b32_e32 v76, 16, v19
	v_pk_mul_f32 v[18:19], v[62:63], v[62:63]
	v_pk_mul_f32 v[78:79], v[28:29], v[28:29]
	v_pk_mul_f32 v[80:81], v[66:67], v[66:67]
	v_pk_mul_f32 v[82:83], v[30:31], v[30:31]
	v_pk_mul_f32 v[84:85], v[70:71], v[70:71]
	v_pk_mul_f32 v[86:87], v[20:21], v[20:21]
	v_pk_mul_f32 v[88:89], v[74:75], v[74:75]
	v_pk_mul_f32 v[90:91], v[22:23], v[22:23]
	s_waitcnt vmcnt(6)
	v_and_b32_e32 v111, 0xffff0000, v46
	s_waitcnt vmcnt(4)
	v_and_b32_e32 v110, 0xffff0000, v50
	v_and_b32_e32 v115, 0xffff0000, v47
	v_and_b32_e32 v114, 0xffff0000, v51
	v_and_b32_e32 v117, 0xffff0000, v48
	v_and_b32_e32 v116, 0xffff0000, v52
	v_and_b32_e32 v119, 0xffff0000, v49
	v_and_b32_e32 v118, 0xffff0000, v53
	s_waitcnt vmcnt(0)
; __device__ __forceinline__ float wave_sum(float v) {
;     v += dpp_mov<0xB1>(v);
;     v += dpp_mov<0x4E>(v);
;     v += dpp_mov<0x141>(v);
;     v += dpp_mov<0x140>(v);
;     const float r0 = __builtin_bit_cast(float, __builtin_amdgcn_readlane(__builtin_bit_cast(int, v), 0)), r1 = __builtin_bit_cast(float, __builtin_amdgcn_readlane(__builtin_bit_cast(int, v), 16));
;     const float r2 = __builtin_bit_cast(float, __builtin_amdgcn_readlane(__builtin_bit_cast(int, v), 32)), r3 = __builtin_bit_cast(float, __builtin_amdgcn_readlane(__builtin_bit_cast(int, v), 48));
;     return (r0 + r1) + (r2 + r3);
; __device__ __forceinline__ float ss_u4(const u32x4& v) {
;     const float a = bflo(v.x), b = bfhi(v.x), c = bflo(v.y), d = bfhi(v.y), e = bflo(v.z), f = bfhi(v.z), g = bflo(v.w), h = bfhi(v.w);
;     return ((a * a + b * b) + (c * c + d * d)) + ((e * e + f * f) + (g * g + h * h)); }
	v_and_b32_e32 v121, 0xffff0000, v58
	v_and_b32_e32 v120, 0xffff0000, v54
	v_and_b32_e32 v123, 0xffff0000, v59
	v_and_b32_e32 v122, 0xffff0000, v55
	v_and_b32_e32 v125, 0xffff0000, v60
	v_and_b32_e32 v124, 0xffff0000, v56
	v_and_b32_e32 v127, 0xffff0000, v61
	v_and_b32_e32 v126, 0xffff0000, v57
	v_mov_b32_e32 v92, v42
	v_mov_b32_e32 v93, v62
	v_mov_b32_e32 v94, v64
	v_mov_b32_e32 v95, v28
	v_mov_b32_e32 v96, v24
	v_mov_b32_e32 v97, v66
	v_mov_b32_e32 v98, v68
	v_mov_b32_e32 v99, v30
	v_mov_b32_e32 v62, v43
	v_mov_b32_e32 v28, v65
	v_mov_b32_e32 v66, v25
	v_mov_b32_e32 v30, v69
	v_mov_b32_e32 v100, v26
	v_mov_b32_e32 v101, v70
	v_mov_b32_e32 v102, v72
	v_mov_b32_e32 v103, v20
	v_mov_b32_e32 v104, v16
	v_mov_b32_e32 v105, v74
	v_mov_b32_e32 v106, v76
	v_mov_b32_e32 v107, v22
	v_mov_b32_e32 v70, v27
	v_mov_b32_e32 v20, v73
	v_mov_b32_e32 v74, v17
	v_mov_b32_e32 v22, v77
	v_lshlrev_b32_e32 v109, 16, v46
	v_lshlrev_b32_e32 v108, 16, v50
	v_lshlrev_b32_e32 v113, 16, v47
	v_lshlrev_b32_e32 v112, 16, v51
	v_lshlrev_b32_e32 v47, 16, v48
	v_lshlrev_b32_e32 v46, 16, v52
	v_lshlrev_b32_e32 v51, 16, v49
	v_lshlrev_b32_e32 v50, 16, v53
	v_lshlrev_b32_e32 v48, 16, v54
	v_lshlrev_b32_e32 v49, 16, v58
	v_lshlrev_b32_e32 v52, 16, v55
	v_lshlrev_b32_e32 v53, 16, v59
	v_lshlrev_b32_e32 v54, 16, v56
	v_lshlrev_b32_e32 v55, 16, v60
	v_lshlrev_b32_e32 v58, 16, v57
	v_lshlrev_b32_e32 v59, 16, v61
	v_pk_fma_f32 v[18:19], v[42:43], v[42:43], v[18:19]
	v_pk_fma_f32 v[42:43], v[64:65], v[64:65], v[78:79]
	v_pk_fma_f32 v[24:25], v[24:25], v[24:25], v[80:81]
	v_pk_fma_f32 v[56:57], v[68:69], v[68:69], v[82:83]
	v_pk_fma_f32 v[26:27], v[26:27], v[26:27], v[84:85]
	v_pk_fma_f32 v[60:61], v[72:73], v[72:73], v[86:87]
	v_pk_fma_f32 v[16:17], v[16:17], v[16:17], v[88:89]
	v_pk_fma_f32 v[64:65], v[76:77], v[76:77], v[90:91]
	v_pk_mul_f32 v[68:69], v[110:111], v[110:111]
	v_pk_mul_f32 v[72:73], v[114:115], v[114:115]
	v_pk_mul_f32 v[76:77], v[116:117], v[116:117]
	v_pk_mul_f32 v[78:79], v[118:119], v[118:119]
	v_pk_mul_f32 v[80:81], v[120:121], v[120:121]
	v_pk_mul_f32 v[82:83], v[122:123], v[122:123]
	v_pk_mul_f32 v[84:85], v[124:125], v[124:125]
	v_pk_mul_f32 v[86:87], v[126:127], v[126:127]
	v_mov_b32_e32 v128, v46
	v_mov_b32_e32 v129, v116
	v_mov_b32_e32 v130, v50
	v_mov_b32_e32 v131, v118
	v_mov_b32_e32 v116, v47
	v_mov_b32_e32 v118, v51
	v_mov_b32_e32 v132, v48
	v_mov_b32_e32 v133, v120
	v_mov_b32_e32 v134, v52
	v_mov_b32_e32 v135, v122
	v_mov_b32_e32 v136, v54
	v_mov_b32_e32 v137, v124
	v_mov_b32_e32 v138, v58
	v_mov_b32_e32 v139, v126
	v_mov_b32_e32 v120, v49
	v_mov_b32_e32 v122, v53
	v_mov_b32_e32 v124, v55
	v_mov_b32_e32 v126, v59
	v_pk_add_f32 v[18:19], v[18:19], v[42:43]
	v_pk_add_f32 v[24:25], v[24:25], v[56:57]
	v_pk_add_f32 v[26:27], v[26:27], v[60:61]
	v_pk_add_f32 v[16:17], v[16:17], v[64:65]
	v_pk_fma_f32 v[42:43], v[108:109], v[108:109], v[68:69]
	v_pk_fma_f32 v[56:57], v[112:113], v[112:113], v[72:73]
	v_pk_fma_f32 v[46:47], v[46:47], v[46:47], v[76:77]
	v_pk_fma_f32 v[50:51], v[50:51], v[50:51], v[78:79]
	v_pk_fma_f32 v[48:49], v[48:49], v[48:49], v[80:81]
	v_pk_fma_f32 v[52:53], v[52:53], v[52:53], v[82:83]
	v_pk_fma_f32 v[54:55], v[54:55], v[54:55], v[84:85]
	v_pk_fma_f32 v[58:59], v[58:59], v[58:59], v[86:87]
	v_pk_add_f32 v[18:19], v[18:19], v[24:25]
	v_pk_add_f32 v[16:17], v[26:27], v[16:17]
	v_pk_add_f32 v[24:25], v[42:43], v[56:57]
	v_pk_add_f32 v[26:27], v[46:47], v[50:51]
	v_pk_add_f32 v[42:43], v[48:49], v[52:53]
	v_pk_add_f32 v[46:47], v[54:55], v[58:59]
	v_add_f32_e32 v48, v18, v19
	v_add_f32_e32 v49, v16, v17
	v_pk_add_f32 v[16:17], v[24:25], v[26:27]
	v_pk_add_f32 v[18:19], v[42:43], v[46:47]
	v_add_f32_dpp v24, v48, v48 quad_perm:[1,0,3,2] row_mask:0xf bank_mask:0xf bound_ctrl:1
	v_add_f32_dpp v25, v49, v49 quad_perm:[1,0,3,2] row_mask:0xf bank_mask:0xf bound_ctrl:1
	v_add_f32_e32 v16, v16, v17
	v_add_f32_e32 v17, v18, v19
	v_add_f32_dpp v18, v24, v24 quad_perm:[2,3,0,1] row_mask:0xf bank_mask:0xf bound_ctrl:1
	v_add_f32_dpp v19, v25, v25 quad_perm:[2,3,0,1] row_mask:0xf bank_mask:0xf bound_ctrl:1
	v_add_f32_dpp v16, v16, v16 quad_perm:[1,0,3,2] row_mask:0xf bank_mask:0xf bound_ctrl:1
	v_add_f32_dpp v17, v17, v17 quad_perm:[1,0,3,2] row_mask:0xf bank_mask:0xf bound_ctrl:1
	v_add_f32_dpp v18, v18, v18 row_half_mirror row_mask:0xf bank_mask:0xf bound_ctrl:1
	v_add_f32_dpp v19, v19, v19 row_half_mirror row_mask:0xf bank_mask:0xf bound_ctrl:1
	v_add_f32_dpp v16, v16, v16 quad_perm:[2,3,0,1] row_mask:0xf bank_mask:0xf bound_ctrl:1
	v_add_f32_dpp v17, v17, v17 quad_perm:[2,3,0,1] row_mask:0xf bank_mask:0xf bound_ctrl:1
	v_add_f32_dpp v18, v18, v18 row_mirror row_mask:0xf bank_mask:0xf bound_ctrl:1
	v_add_f32_dpp v19, v19, v19 row_mirror row_mask:0xf bank_mask:0xf bound_ctrl:1
	v_add_f32_dpp v16, v16, v16 row_half_mirror row_mask:0xf bank_mask:0xf bound_ctrl:1
	v_add_f32_dpp v17, v17, v17 row_half_mirror row_mask:0xf bank_mask:0xf bound_ctrl:1
	v_readlane_b32 s4, v18, 16
	v_readlane_b32 s5, v18, 48
	v_readlane_b32 s17, v19, 16
	v_readlane_b32 s18, v19, 48
	v_add_f32_dpp v24, v16, v16 row_mirror row_mask:0xf bank_mask:0xf bound_ctrl:1
	v_add_f32_dpp v25, v17, v17 row_mirror row_mask:0xf bank_mask:0xf bound_ctrl:1
	v_readlane_b32 s0, v18, 0
	v_readlane_b32 s1, v18, 32
	v_readlane_b32 s2, v19, 0
	v_readlane_b32 s3, v19, 32
	v_mov_b32_e32 v16, s4
	v_mov_b32_e32 v17, s5
	v_mov_b32_e32 v18, s17
	v_mov_b32_e32 v19, s18
	v_readlane_b32 s17, v24, 16
	v_readlane_b32 s20, v24, 48
	v_readlane_b32 s21, v25, 16
	v_readlane_b32 s22, v25, 48
	v_readlane_b32 s4, v24, 0
	v_readlane_b32 s5, v24, 32
	v_readlane_b32 s18, v25, 0
	v_readlane_b32 s19, v25, 32
; __device__ __forceinline__ void phase_final(const bf16* H, float* out, const float* gain, int gw, int NGW, int lane) {
;     ...
;     for (int m0 = gw * NR; m0 < NTOK; m0 += NGW * NR) { u32x4 v[NR][2];
; #pragma unroll
;         for (int r = 0; r < NR; ++r)
; #pragma unroll
;             for (int j = 0; j < 2; ++j) v[r][j] = ((const u32x4*)(H + (size_t)(m0 + r) * DM))[lane + 64 * j];
; #pragma unroll
;         for (int r = 0; r < NR; ++r) { const float rstd = rsqrtf(wave_sum(ss_u4(v[r][0]) + ss_u4(v[r][1])) * (1.f / DM) + EPS);
;             f32x4* xr = (f32x4*)(out + (size_t)(m0 + r) * DM);
; #pragma unroll
;             for (int j = 0; j < 2; ++j) { const u32x4 w = v[r][j];
;                 xr[2 * lane + 128 * j] = (f32x4){bflo(w.x), bfhi(w.x), bflo(w.y), bfhi(w.y)} * rstd * gv[j][0];
;                 xr[2 * lane + 128 * j + 1] = (f32x4){bflo(w.z), bfhi(w.z), bflo(w.w), bfhi(w.w)} * rstd * gv[j][1]; } } }
	v_pk_add_f32 v[16:17], s[0:1], v[16:17]
	v_pk_add_f32 v[18:19], s[2:3], v[18:19]
	v_mov_b32_e32 v24, s17
	v_mov_b32_e32 v25, s20
	v_mov_b32_e32 v26, s21
	v_mov_b32_e32 v27, s22
	v_mov_b32_e32 v42, v18
	v_mov_b32_e32 v43, v16
	v_mov_b32_e32 v16, v19
	v_pk_add_f32 v[18:19], s[4:5], v[24:25]
	v_pk_add_f32 v[24:25], s[18:19], v[26:27]
	v_pk_add_f32 v[16:17], v[42:43], v[16:17]
	v_mov_b32_e32 v26, v24
	v_mov_b32_e32 v27, v18
	v_mov_b32_e32 v18, v25
	v_pk_fma_f32 v[16:17], v[16:17], s[14:15], v[36:37] op_sel_hi:[1,0,0]
	v_pk_add_f32 v[18:19], v[26:27], v[18:19]
	v_mul_f32_e32 v24, 0x4b800000, v17
	v_mul_f32_e32 v25, 0x4b800000, v16
	v_cmp_gt_f32_e32 vcc, s9, v16
	v_cmp_gt_f32_e64 s[0:1], s9, v17
	v_pk_fma_f32 v[18:19], v[18:19], s[14:15], v[36:37] op_sel_hi:[1,0,0]
	v_cndmask_b32_e32 v16, v16, v25, vcc
	v_cndmask_b32_e64 v17, v17, v24, s[0:1]
	v_mul_f32_e32 v24, 0x4b800000, v19
	v_cmp_gt_f32_e64 s[4:5], s9, v19
	v_mul_f32_e32 v25, 0x4b800000, v18
	v_cmp_gt_f32_e64 s[2:3], s9, v18
	v_rsq_f32_e32 v17, v17
	v_rsq_f32_e32 v26, v16
	v_cndmask_b32_e64 v16, v19, v24, s[4:5]
	v_cndmask_b32_e64 v18, v18, v25, s[2:3]
	v_rsq_f32_e32 v19, v16
	v_rsq_f32_e32 v69, v18
	v_mul_f32_e32 v16, 0x45800000, v17
	v_mul_f32_e32 v18, 0x45800000, v26
	v_cndmask_b32_e64 v16, v17, v16, s[0:1]
	v_cndmask_b32_e32 v18, v26, v18, vcc
	v_mul_f32_e32 v17, 0x45800000, v19
	v_mov_b32_e32 v88, v108
	v_mov_b32_e32 v89, v110
	v_mov_b32_e32 v90, v112
	v_mov_b32_e32 v91, v114
	v_mul_f32_e32 v72, 0x45800000, v69
	v_pk_mul_f32 v[24:25], v[16:17], v[92:93] op_sel_hi:[0,1]
	v_pk_mul_f32 v[26:27], v[16:17], v[94:95] op_sel_hi:[0,1]
	v_pk_mul_f32 v[42:43], v[16:17], v[96:97] op_sel_hi:[0,1]
	v_pk_mul_f32 v[48:49], v[16:17], v[62:63] op_sel_hi:[0,1]
	v_pk_mul_f32 v[28:29], v[16:17], v[28:29] op_sel_hi:[0,1]
	v_pk_mul_f32 v[50:51], v[16:17], v[66:67] op_sel_hi:[0,1]
	v_pk_mul_f32 v[56:57], v[18:19], v[104:105] op_sel_hi:[0,1]
	v_pk_mul_f32 v[62:63], v[18:19], v[20:21] op_sel_hi:[0,1]
	v_cndmask_b32_e64 v68, v19, v17, s[4:5]
	v_mov_b32_e32 v110, v109
	v_mov_b32_e32 v114, v113
	v_pk_mul_f32 v[46:47], v[16:17], v[98:99] op_sel_hi:[0,1]
	v_pk_mul_f32 v[30:31], v[16:17], v[30:31] op_sel_hi:[0,1]
	v_pk_mul_f32 v[52:53], v[18:19], v[100:101] op_sel_hi:[0,1]
	v_pk_mul_f32 v[54:55], v[18:19], v[102:103] op_sel_hi:[0,1]
	v_pk_mul_f32 v[58:59], v[18:19], v[106:107] op_sel_hi:[0,1]
	v_pk_mul_f32 v[60:61], v[18:19], v[70:71] op_sel_hi:[0,1]
	v_pk_mul_f32 v[64:65], v[18:19], v[74:75] op_sel_hi:[0,1]
	v_pk_mul_f32 v[66:67], v[18:19], v[22:23] op_sel_hi:[0,1]
	v_cndmask_b32_e64 v70, v69, v72, s[2:3]
	v_pk_mul_f32 v[18:19], v[6:7], v[26:27]
	v_pk_mul_f32 v[16:17], v[4:5], v[24:25]
	v_pk_mul_f32 v[20:21], v[0:1], v[42:43]
	v_pk_mul_f32 v[26:27], v[14:15], v[28:29]
	v_pk_mul_f32 v[28:29], v[8:9], v[50:51]
	v_pk_mul_f32 v[50:51], v[0:1], v[56:57]
	v_pk_mul_f32 v[56:57], v[14:15], v[62:63]
	v_pk_mul_f32 v[42:43], v[68:69], v[88:89] op_sel_hi:[0,1]
	v_pk_mul_f32 v[62:63], v[68:69], v[90:91] op_sel_hi:[0,1]
	v_pk_mul_f32 v[22:23], v[2:3], v[46:47]
	v_pk_mul_f32 v[24:25], v[12:13], v[48:49]
	v_pk_mul_f32 v[30:31], v[10:11], v[30:31]
	v_pk_mul_f32 v[48:49], v[6:7], v[54:55]
	v_pk_mul_f32 v[46:47], v[4:5], v[52:53]
	v_pk_mul_f32 v[52:53], v[2:3], v[58:59]
	v_pk_mul_f32 v[54:55], v[12:13], v[60:61]
	v_pk_mul_f32 v[60:61], v[10:11], v[66:67]
	v_pk_mul_f32 v[58:59], v[8:9], v[64:65]
	v_pk_mul_f32 v[64:65], v[68:69], v[128:129] op_sel_hi:[0,1]
	v_pk_mul_f32 v[66:67], v[68:69], v[130:131] op_sel_hi:[0,1]
	v_pk_mul_f32 v[72:73], v[68:69], v[110:111] op_sel_hi:[0,1]
	v_pk_mul_f32 v[74:75], v[68:69], v[114:115] op_sel_hi:[0,1]
	v_pk_mul_f32 v[76:77], v[68:69], v[116:117] op_sel_hi:[0,1]
	v_pk_mul_f32 v[68:69], v[68:69], v[118:119] op_sel_hi:[0,1]
	v_pk_mul_f32 v[78:79], v[70:71], v[132:133] op_sel_hi:[0,1]
	v_pk_mul_f32 v[80:81], v[70:71], v[134:135] op_sel_hi:[0,1]
	v_pk_mul_f32 v[82:83], v[70:71], v[136:137] op_sel_hi:[0,1]
	v_pk_mul_f32 v[84:85], v[70:71], v[138:139] op_sel_hi:[0,1]
	v_pk_mul_f32 v[86:87], v[70:71], v[120:121] op_sel_hi:[0,1]
	v_pk_mul_f32 v[88:89], v[70:71], v[122:123] op_sel_hi:[0,1]
	v_pk_mul_f32 v[90:91], v[70:71], v[124:125] op_sel_hi:[0,1]
	v_pk_mul_f32 v[70:71], v[70:71], v[126:127] op_sel_hi:[0,1]
	global_store_dwordx4 v[44:45], v[16:19], off offset:-2064
	global_store_dwordx4 v[44:45], v[20:23], off offset:-1040
	global_store_dwordx4 v[44:45], v[24:27], off offset:-16
	global_store_dwordx4 v[32:33], v[28:31], off offset:-3088
	global_store_dwordx4 v[32:33], v[46:49], off offset:-2064
	global_store_dwordx4 v[32:33], v[50:53], off offset:-1040
	global_store_dwordx4 v[32:33], v[54:57], off offset:-16
	global_store_dwordx4 v[32:33], v[58:61], off offset:1008
	v_lshl_add_u64 v[32:33], v[32:33], 0, s[10:11]
	v_pk_mul_f32 v[18:19], v[6:7], v[62:63]
	v_pk_mul_f32 v[16:17], v[4:5], v[42:43]
	v_pk_mul_f32 v[22:23], v[2:3], v[66:67]
	v_pk_mul_f32 v[20:21], v[0:1], v[64:65]
	v_pk_mul_f32 v[26:27], v[14:15], v[74:75]
	v_pk_mul_f32 v[24:25], v[12:13], v[72:73]
	v_pk_mul_f32 v[30:31], v[10:11], v[68:69]
	v_pk_mul_f32 v[28:29], v[8:9], v[76:77]
	v_pk_mul_f32 v[44:45], v[6:7], v[80:81]
	v_pk_mul_f32 v[42:43], v[4:5], v[78:79]
	v_pk_mul_f32 v[48:49], v[2:3], v[84:85]
	v_pk_mul_f32 v[46:47], v[0:1], v[82:83]
	v_pk_mul_f32 v[52:53], v[14:15], v[88:89]
	v_pk_mul_f32 v[50:51], v[12:13], v[86:87]
	v_pk_mul_f32 v[56:57], v[10:11], v[70:71]
	v_pk_mul_f32 v[54:55], v[8:9], v[90:91]
	global_store_dwordx4 v[38:39], v[16:19], off offset:-2064
	global_store_dwordx4 v[38:39], v[20:23], off offset:-1040
	global_store_dwordx4 v[38:39], v[24:27], off offset:-16
	global_store_dwordx4 v[40:41], v[28:31], off offset:-3088
	global_store_dwordx4 v[40:41], v[42:45], off offset:-2064
	global_store_dwordx4 v[40:41], v[46:49], off offset:-1040
	global_store_dwordx4 v[40:41], v[50:53], off offset:-16
	global_store_dwordx4 v[40:41], v[54:57], off offset:1008
	s_cbranch_scc1 .LBB0_1268
